# speedup vs baseline: 1.0068x; 1.0017x over previous
.LBB1_49:
	s_or_b64 exec, exec, s[0:1]
	s_lshl_b32 s0, s33, 2
	s_add_u32 s0, s38, s0
	s_addc_u32 s1, s39, 0
	s_mov_b32 s2, 0x138800
	s_mov_b32 s18, 0
	v_lshlrev_b32_e32 v1, 1, v0
	v_xor_b32_e32 v8, 0x7fe, v1
	v_lshlrev_b32_e32 v9, 2, v8
	v_mov_b32_e32 v5, v4
	v_cmp_gt_u32_e32 vcc, 8, v0
	v_lshlrev_b32_e32 v27, 2, v0
	ds_write_b64 v9, v[4:5]
	s_and_saveexec_b64 s[0:1], vcc
	v_mov_b32_e32 v1, 0
	ds_write_b32 v27, v1 offset:8192
	s_or_b64 exec, exec, s[0:1]
	v_cmp_gt_u32_e64 s[0:1], 17, v0
	s_and_saveexec_b64 s[2:3], s[0:1]
	v_mov_b32_e32 v1, 0
	ds_write_b32 v27, v1 offset:48288
	s_or_b64 exec, exec, s[2:3]
	v_lshrrev_b32_e32 v34, 6, v0
	v_and_b32_e32 v1, 63, v0
	s_waitcnt lgkmcnt(0)
	s_barrier
	v_cmp_gt_u32_e32 vcc, 17, v1
	v_cmp_gt_u32_e64 s[2:3], v1, v34
	s_and_b64 s[16:17], vcc, s[2:3]
	s_waitcnt vmcnt(3)
	v_cmp_ne_u32_e64 s[14:15], 0, v2
	s_waitcnt vmcnt(2)
	v_cmp_ne_u32_e64 s[12:13], 0, v24
	s_waitcnt vmcnt(1)
	v_cmp_ne_u32_e64 s[10:11], 0, v22
	s_waitcnt vmcnt(0)
	v_cmp_ne_u32_e64 s[6:7], 0, v20
	v_cmp_ne_u32_e64 s[4:5], 0, v18
	v_mov_b32_e32 v4, 0
	v_lshlrev_b32_e32 v30, 2, v34
	v_lshlrev_b32_e32 v15, 2, v1
	v_mov_b32_e32 v16, 1
	s_movk_i32 s22, 0x12c
	v_mov_b32_e32 v5, v4
	s_branch .LBB1_56

.LBB1_56:
	s_mov_b32 s20, 0x3c000000
	s_mov_b32 s21, 15
	v_subrev_u32_e32 v6, s20, v2
	v_lshrrev_b32_e32 v6, 13, v6
	v_and_b32_e32 v14, 0x1ffc, v6
	v_subrev_u32_e32 v6, s20, v24
	v_lshrrev_b32_e32 v6, 13, v6
	v_and_b32_e32 v13, 0x1ffc, v6
	v_subrev_u32_e32 v6, s20, v22
	v_lshrrev_b32_e32 v6, 13, v6
	v_and_b32_e32 v12, 0x1ffc, v6
	v_subrev_u32_e32 v6, s20, v20
	v_lshrrev_b32_e32 v6, 13, v6
	v_and_b32_e32 v11, 0x1ffc, v6
	v_subrev_u32_e32 v6, s20, v18
	v_lshrrev_b32_e32 v6, 13, v6
	v_and_b32_e32 v10, 0x1ffc, v6
	s_mov_b64 exec, s[14:15]
	ds_add_u32 v14, v16
	s_mov_b64 exec, s[12:13]
	ds_add_u32 v13, v16
	s_mov_b64 exec, s[10:11]
	ds_add_u32 v12, v16
	s_mov_b64 exec, s[6:7]
	ds_add_u32 v11, v16
	s_mov_b64 exec, s[4:5]
	ds_add_u32 v10, v16
	s_mov_b64 exec, -1
	s_waitcnt lgkmcnt(0)
	s_barrier
	ds_read_b64 v[6:7], v9
	s_waitcnt lgkmcnt(0)
	v_add_u32_e32 v17, v7, v6
	s_nop 1
	v_add_u32_dpp v26, v17, v17 row_shr:1 row_mask:0xf bank_mask:0xf bound_ctrl:1
	s_nop 1
	v_add_u32_dpp v26, v26, v26 row_shr:2 row_mask:0xf bank_mask:0xf bound_ctrl:1
	s_nop 1
	v_add_u32_dpp v26, v26, v26 row_shr:4 row_mask:0xf bank_mask:0xf bound_ctrl:1
	s_nop 1
	v_add_u32_dpp v26, v26, v26 row_shr:8 row_mask:0xf bank_mask:0xf bound_ctrl:1
	s_nop 1
	v_add_u32_dpp v26, v26, v26 row_bcast:15 row_mask:0xa bank_mask:0xf
	s_nop 1
	v_add_u32_dpp v26, v26, v26 row_bcast:31 row_mask:0xc bank_mask:0xf
	s_nop 0
	v_readlane_b32 s8, v26, 63
	s_and_saveexec_b64 s[2:3], s[16:17]
	s_nop 0
	v_mov_b32_e32 v32, s8
	ds_add_u32 v15, v32 offset:48288
	s_or_b64 exec, exec, s[2:3]
	s_waitcnt lgkmcnt(0)
	s_barrier
	ds_read_b32 v32, v4 offset:48352
	ds_read_b32 v35, v30 offset:48288
	s_cmp_eq_u32 s18, 0
	s_cselect_b64 s[8:9], -1, 0
	s_waitcnt lgkmcnt(1)
	v_cmp_lt_i32_e64 s[2:3], s22, v32
	s_or_b64 s[8:9], s[8:9], s[2:3]
	s_and_b64 vcc, exec, s[8:9]
	s_cbranch_vccnz .LBB1_55
	s_waitcnt lgkmcnt(0)
	s_barrier
	ds_write_b64 v9, v[4:5]
	s_and_saveexec_b64 s[18:19], s[0:1]
	s_cbranch_execz .LBB1_54
	ds_write_b32 v27, v4 offset:48288
	s_branch .LBB1_54

.LBB1_74:
	s_or_b64 exec, exec, s[0:1]
	v_mov_b32_e32 v4, 0
	s_waitcnt lgkmcnt(0)
	s_barrier
	ds_read_b64 v[4:5], v4 offset:48432
	v_lshlrev_b32_e32 v6, 7, v0
	s_mov_b64 s[0:1], exec
	s_waitcnt lgkmcnt(0)
	v_lshlrev_b32_e32 v4, 2, v4
	v_cmp_ge_u32_e32 vcc, v14, v4
	s_and_b64 s[14:15], s[14:15], vcc
	v_cmp_ge_u32_e32 vcc, v13, v4
	s_and_b64 s[12:13], s[12:13], vcc
	v_cmp_ge_u32_e32 vcc, v12, v4
	s_and_b64 s[10:11], s[10:11], vcc
	v_cmp_ge_u32_e32 vcc, v11, v4
	s_and_b64 s[6:7], s[6:7], vcc
	v_cmp_ge_u32_e32 vcc, v10, v4
	s_and_b64 s[4:5], s[4:5], vcc
	v_mov_b32_e32 v7, 1
	s_mov_b64 exec, s[14:15]
	ds_add_rtn_u32 v58, v14, v7
	s_mov_b64 exec, s[12:13]
	ds_add_rtn_u32 v59, v13, v7
	s_mov_b64 exec, s[10:11]
	ds_add_rtn_u32 v60, v12, v7
	s_mov_b64 exec, s[6:7]
	ds_add_rtn_u32 v61, v11, v7
	s_mov_b64 exec, s[4:5]
	ds_add_rtn_u32 v62, v10, v7
	s_mov_b64 exec, s[0:1]
	s_waitcnt lgkmcnt(0)
	v_sub_u32_e32 v8, 0xfff80, v6
	v_or_b32_e32 v8, v3, v8
	v_mov_b32_e32 v9, v2
	v_lshlrev_b32_e32 v58, 3, v58
	s_mov_b64 exec, s[14:15]
	ds_write_b64 v58, v[8:9] offset:8224
	s_mov_b64 exec, s[0:1]
	v_sub_u32_e32 v8, 0xdff80, v6
	v_or_b32_e32 v8, v25, v8
	v_mov_b32_e32 v9, v24
	v_lshlrev_b32_e32 v59, 3, v59
	s_mov_b64 exec, s[12:13]
	ds_write_b64 v59, v[8:9] offset:8224
	s_mov_b64 exec, s[0:1]
	v_sub_u32_e32 v8, 0xbff80, v6
	v_or_b32_e32 v8, v23, v8
	v_mov_b32_e32 v9, v22
	v_lshlrev_b32_e32 v60, 3, v60
	s_mov_b64 exec, s[10:11]
	ds_write_b64 v60, v[8:9] offset:8224
	s_mov_b64 exec, s[0:1]
	v_sub_u32_e32 v8, 0x9ff80, v6
	v_or_b32_e32 v8, v21, v8
	v_mov_b32_e32 v9, v20
	v_lshlrev_b32_e32 v61, 3, v61
	s_mov_b64 exec, s[6:7]
	ds_write_b64 v61, v[8:9] offset:8224
	s_mov_b64 exec, s[0:1]
	v_sub_u32_e32 v8, 0x7ff80, v6
	v_or_b32_e32 v8, v19, v8
	v_mov_b32_e32 v9, v18
	v_lshlrev_b32_e32 v62, 3, v62
	s_mov_b64 exec, s[4:5]
	ds_write_b64 v62, v[8:9] offset:8224
	s_mov_b64 exec, s[0:1]
	v_cmp_lt_i32_e32 vcc, v0, v5
	s_waitcnt lgkmcnt(0)
	s_barrier
	s_and_saveexec_b64 s[0:1], vcc
	s_cbranch_execz .LBB1_93
	s_mov_b64 s[2:3], 0
	s_movk_i32 s8, 0x12c
	s_mov_b32 s9, 0x51eb851f
	s_movk_i32 s10, 0xff9c
	s_mov_b32 s11, 0x43480000
	s_mov_b32 s12, 0x43c80000
	s_mov_b32 s13, 0x3ba3d70a
	s_mov_b32 s14, 0x3b23d70a
	v_mov_b32_e32 v4, 1.0
	v_mov_b32_e32 v10, 0x2020
	v_mov_b32_e32 v11, v0
	s_branch .LBB1_87
